# speedup vs baseline: 1.0369x; 1.0010x over previous
.Lkv_tail_done:
	s_waitcnt vmcnt(0)
	s_barrier
	s_and_saveexec_b64 s[52:53], s[56:57]
	s_cbranch_execz .Lkv_noarrive
	v_mov_b32_e32 v228, 0
	v_mov_b32_e32 v229, 1
	global_atomic_add v228, v229, s[54:55] sc1
.Lkv_noarrive:
	s_or_b64 exec, exec, s[52:53]
	s_waitcnt lgkmcnt(0)
	s_setprio 1
	s_waitcnt lgkmcnt(0)
	v_mfma_f32_16x16x32_f16 v[102:105], v[194:197], v[18:21], v[210:213]
	v_mfma_f32_16x16x32_f16 v[18:21], v[206:209], v[18:21], v[166:169]
	v_mfma_f32_16x16x32_f16 v[114:117], v[218:221], v[26:29], v[18:21]
	v_mfma_f32_16x16x32_f16 v[18:21], v[194:197], v[30:33], v[214:217]
	v_mfma_f32_16x16x32_f16 v[110:113], v[202:205], v[26:29], v[102:105]
	v_mfma_f32_16x16x32_f16 v[102:105], v[202:205], v[50:53], v[18:21]
	v_mfma_f32_16x16x32_f16 v[18:21], v[206:209], v[30:33], v[82:85]
	v_mfma_f32_16x16x32_f16 v[106:109], v[218:221], v[50:53], v[18:21]
	v_mfma_f32_16x16x32_f16 v[18:21], v[194:197], v[58:61], v[78:81]
	v_mfma_f32_16x16x32_f16 v[78:81], v[202:205], v[178:181], v[18:21]
	v_mfma_f32_16x16x32_f16 v[18:21], v[206:209], v[58:61], v[74:77]
	v_mfma_f32_16x16x32_f16 v[82:85], v[218:221], v[178:181], v[18:21]
	v_mfma_f32_16x16x32_f16 v[18:21], v[194:197], v[182:185], v[70:73]
	v_mfma_f32_16x16x32_f16 v[70:73], v[202:205], v[198:201], v[18:21]
	v_mfma_f32_16x16x32_f16 v[18:21], v[206:209], v[182:185], v[66:69]
	v_mfma_f32_16x16x32_f16 v[74:77], v[218:221], v[198:201], v[18:21]
	s_setprio 0
	s_barrier
	ds_read_b128 v[66:69], v138 offset:49152
	ds_read_b128 v[164:167], v138 offset:50176
	ds_read_b128 v[178:181], v137 offset:49152
	ds_read_b128 v[182:185], v137 offset:50176
	ds_read_b128 v[198:201], v136 offset:49152
	ds_read_b128 v[136:139], v136 offset:50176
	ds_read_b128 v[210:213], v135 offset:49152
	ds_read_b128 v[214:217], v135 offset:50176
	s_barrier
	s_waitcnt lgkmcnt(0)
	s_setprio 1
	s_waitcnt lgkmcnt(0)
	v_mfma_f32_16x16x32_f16 v[18:21], v[2:5], v[66:69], v[62:65]
	v_mfma_f32_16x16x32_f16 v[58:61], v[10:13], v[164:167], v[18:21]
	v_mfma_f32_16x16x32_f16 v[18:21], v[22:25], v[66:69], v[186:189]
	v_mfma_f32_16x16x32_f16 v[62:65], v[140:143], v[164:167], v[18:21]
	v_mfma_f32_16x16x32_f16 v[18:21], v[2:5], v[178:181], v[54:57]
	v_mfma_f32_16x16x32_f16 v[50:53], v[10:13], v[182:185], v[18:21]
	v_mfma_f32_16x16x32_f16 v[18:21], v[22:25], v[178:181], v[190:193]
	v_mfma_f32_16x16x32_f16 v[54:57], v[140:143], v[182:185], v[18:21]
	v_mfma_f32_16x16x32_f16 v[18:21], v[2:5], v[198:201], v[46:49]
	v_mfma_f32_16x16x32_f16 v[26:29], v[10:13], v[136:139], v[18:21]
	v_mfma_f32_16x16x32_f16 v[18:21], v[22:25], v[198:201], v[42:45]
	v_mfma_f32_16x16x32_f16 v[2:5], v[2:5], v[210:213], v[38:41]
	v_mfma_f32_16x16x32_f16 v[30:33], v[140:143], v[136:139], v[18:21]
	v_mfma_f32_16x16x32_f16 v[18:21], v[10:13], v[214:217], v[2:5]
	v_mfma_f32_16x16x32_f16 v[2:5], v[22:25], v[210:213], v[34:37]
	v_mfma_f32_16x16x32_f16 v[22:25], v[140:143], v[214:217], v[2:5]
	s_setprio 0
	s_setprio 1
	v_mfma_f32_16x16x32_f16 v[2:5], v[194:197], v[66:69], v[148:151]
	v_mfma_f32_16x16x32_f16 v[42:45], v[202:205], v[164:167], v[2:5]
	v_mfma_f32_16x16x32_f16 v[2:5], v[206:209], v[66:69], v[152:155]
	v_mfma_f32_16x16x32_f16 v[46:49], v[218:221], v[164:167], v[2:5]
	v_mfma_f32_16x16x32_f16 v[2:5], v[194:197], v[178:181], v[156:159]
	v_mfma_f32_16x16x32_f16 v[34:37], v[202:205], v[182:185], v[2:5]
	v_mfma_f32_16x16x32_f16 v[2:5], v[206:209], v[178:181], v[160:163]
	v_mfma_f32_16x16x32_f16 v[38:41], v[218:221], v[182:185], v[2:5]
	v_mfma_f32_16x16x32_f16 v[2:5], v[194:197], v[198:201], v[14:17]
	v_mfma_f32_16x16x32_f16 v[10:13], v[202:205], v[136:139], v[2:5]
	v_mfma_f32_16x16x32_f16 v[2:5], v[206:209], v[198:201], v[170:173]
	v_mfma_f32_16x16x32_f16 v[14:17], v[218:221], v[136:139], v[2:5]
	v_mfma_f32_16x16x32_f16 v[2:5], v[194:197], v[210:213], v[6:9]
	v_mfma_f32_16x16x32_f16 v[6:9], v[206:209], v[210:213], v[174:177]
	v_mfma_f32_16x16x32_f16 v[2:5], v[202:205], v[214:217], v[2:5]
	v_mfma_f32_16x16x32_f16 v[6:9], v[218:221], v[214:217], v[6:9]
	s_setprio 0
	s_movk_i32 s0, 0x100
	v_cmp_gt_u32_e32 vcc, s0, v0
	s_barrier
	s_and_saveexec_b64 s[0:1], vcc
	s_cbranch_execz .LBB2_62
	s_barrier
